# static s_setprio 1 for the older wave half (waves 0-3) in the non-GEMM MFMA phases: the per-half A/B of the priority raise
# baseline (speedup 1.0000x reference)
.LBB0_607:
	s_or_b64 exec, exec, s[0:1]
	s_waitcnt lgkmcnt(0)
	s_barrier
	v_cmp_gt_u32_e32 vcc, 0x100, v0
	s_cbranch_vccz .Lprio_1
	s_setprio 1
